# topk_bitsearch_early_exit_when_count_equals_capacity
# baseline (speedup 1.0000x reference)
.LBB0_787:
	s_or_b64 exec, exec, s[30:31]
	v_readlane_b32 s4, v253, 40
	v_mov_b32_e32 v135, v0
	s_mov_b64 s[0:1], 0
	s_mov_b32 s24, s37
	v_readlane_b32 s27, v253, 8
	v_readlane_b32 s18, v253, 54
	s_waitcnt lgkmcnt(0)
	s_barrier
	v_readlane_b32 s19, v253, 55
	s_add_u32 s62, s18, s0
	s_addc_u32 s26, s19, s1
	v_and_b32_e32 v132, 63, v135
	s_cmp_lt_i32 s27, 32
	s_mov_b64 s[0:1], -1
	v_readlane_b32 s5, v253, 41
	v_readlane_b32 s6, v253, 42
	v_readlane_b32 s7, v253, 43
	v_readlane_b32 s8, v253, 44
	v_readlane_b32 s9, v253, 45
	v_readlane_b32 s10, v253, 46
	v_readlane_b32 s11, v253, 47
	v_readlane_b32 s12, v253, 48
	v_readlane_b32 s13, v253, 49
	v_readlane_b32 s14, v253, 50
	v_readlane_b32 s15, v253, 51
	v_readlane_b32 s16, v253, 52
	v_readlane_b32 s17, v253, 53
	s_cbranch_scc0 .LBB0_876
	s_and_b32 s37, s27, 1
	s_ashr_i32 s25, s27, 1
	s_lshl_b32 s0, s37, 4
	s_add_i32 s0, s0, s25
	s_ashr_i32 s1, s0, 31
	s_lshl_b64 s[0:1], s[0:1], 16
	s_add_u32 s0, s62, s0
	v_lshlrev_b32_e32 v34, 5, v135
	s_addc_u32 s1, s26, s1
	v_ashrrev_i32_e32 v35, 31, v34
	v_lshl_add_u64 v[2:3], v[34:35], 2, s[0:1]
	s_mov_b64 s[0:1], 0x200000
	v_lshl_add_u64 v[4:5], v[2:3], 0, s[0:1]
	s_mov_b32 s0, 0x200000
	v_add_co_u32_e32 v2, vcc, s0, v2
	s_mov_b32 s2, 0
	s_nop 0
	v_addc_co_u32_e32 v3, vcc, 0, v3, vcc
	global_load_dwordx4 v[26:29], v[4:5], off offset:16
	global_load_dwordx4 v[22:25], v[4:5], off offset:32
	global_load_dwordx4 v[18:21], v[4:5], off offset:48
	global_load_dwordx4 v[14:17], v[4:5], off offset:64
	global_load_dwordx4 v[10:13], v[4:5], off offset:80
	global_load_dwordx4 v[6:9], v[4:5], off offset:96
	global_load_dwordx4 v[30:33], v[2:3], off
	s_nop 0
	global_load_dwordx4 v[2:5], v[4:5], off offset:112
	v_cmp_eq_u32_e32 vcc, 0, v132
	s_mov_b32 s3, 29
	v_mov_b32_e32 v45, 0
	s_branch .LBB0_790
.LBB0_789:
	s_or_b64 exec, exec, s[0:1]
	v_mov_b32_e32 v40, s4
	s_waitcnt lgkmcnt(0)
	s_barrier
	ds_read_b128 v[36:39], v40
	ds_read_b128 v[40:43], v40 offset:16
	s_movk_i32 s0, 0x7ff
	s_add_i32 s3, s3, -1
	s_add_i32 s2, s2, 8
	s_waitcnt lgkmcnt(1)
	v_add_u32_e32 v36, v37, v36
	v_add_u32_e32 v36, v36, v38
	v_add_u32_e32 v36, v36, v39
	s_waitcnt lgkmcnt(0)
	v_add_u32_e32 v36, v36, v40
	v_add_u32_e32 v36, v36, v41
	v_add_u32_e32 v36, v36, v42
	v_add_u32_e32 v36, v36, v43
	v_cmp_lt_i32_e64 s[0:1], s0, v36
	v_readfirstlane_b32 s5, v36
	s_cmpk_eq_i32 s5, 0x800
	s_cbranch_scc1 .Ltopk_early
	s_cmp_eq_u32 s3, -1
	s_nop 0
	v_cndmask_b32_e64 v45, v45, v35, s[0:1]
	s_cbranch_scc1 .LBB0_792

.Ltopk_early:
	v_add_u32_e32 v45, -1, v35
